# baseline (speedup 1.0000x reference)
_Z6gat_k2PKDF16_S0_S0_PKfPf:
	s_load_dwordx8 s[4:11], s[0:1], 0x0
	s_load_dwordx2 s[12:13], s[0:1], 0x20
	v_readfirstlane_b32 s14, v0
	v_and_b32_e32 v46, 63, v0
	v_lshlrev_b32_e32 v1, 4, v46
	s_and_b32 s16, s2, 1
	s_bfe_u32 s17, s2, 0x60003
	s_lshr_b32 s18, s2, 1
	s_lshr_b32 s15, s14, 6
	s_lshl_b32 s19, s16, 19
	s_lshl_b32 s23, s15, 16
	s_add_u32 s19, s19, s23
	s_lshl_b32 s23, s15, 11
	v_add_u32_e32 v47, s23, v1
	v_and_b32_e32 v44, 31, v0
	v_lshlrev_b32_e32 v45, 2, v44
	s_lshl_b32 s23, s18, 8
	v_add_u32_e32 v45, s23, v45
	s_waitcnt lgkmcnt(0)
	global_load_dword v42, v45, s[10:11]
	global_load_dword v43, v45, s[10:11] offset:128
	global_load_dwordx4 v[48:51], v47, s[6:7]
	global_load_dwordx4 v[52:55], v47, s[6:7] offset:1024
	global_load_dwordx4 v[56:59], v47, s[8:9]
	global_load_dwordx4 v[60:63], v47, s[8:9] offset:1024
	s_add_u32 s20, s4, s19
	s_addc_u32 s21, s5, 0
	s_add_u32 s23, s17, 0
	s_and_b32 s23, s23, 63
	s_lshl_b32 s23, s23, 10
	s_add_u32 s24, s20, s23
	s_addc_u32 s25, s21, 0
	global_load_dwordx4 v[64:67], v1, s[24:25]
	s_add_u32 s23, s17, 1
	s_and_b32 s23, s23, 63
	s_lshl_b32 s23, s23, 10
	s_add_u32 s24, s20, s23
	s_addc_u32 s25, s21, 0
	global_load_dwordx4 v[68:71], v1, s[24:25]
	s_add_u32 s23, s17, 2
	s_and_b32 s23, s23, 63
	s_lshl_b32 s23, s23, 10
	s_add_u32 s24, s20, s23
	s_addc_u32 s25, s21, 0
	global_load_dwordx4 v[72:75], v1, s[24:25]
	s_add_u32 s23, s17, 3
	s_and_b32 s23, s23, 63
	s_lshl_b32 s23, s23, 10
	s_add_u32 s24, s20, s23
	s_addc_u32 s25, s21, 0
	global_load_dwordx4 v[76:79], v1, s[24:25]
	v_accvgpr_write_b32 a0, 0
	v_accvgpr_write_b32 a1, 0
	v_accvgpr_write_b32 a2, 0
	v_accvgpr_write_b32 a3, 0
	v_accvgpr_write_b32 a4, 0
	v_accvgpr_write_b32 a5, 0
	v_accvgpr_write_b32 a6, 0
	v_accvgpr_write_b32 a7, 0
	v_accvgpr_write_b32 a8, 0
	v_accvgpr_write_b32 a9, 0
	v_accvgpr_write_b32 a10, 0
	v_accvgpr_write_b32 a11, 0
	v_accvgpr_write_b32 a12, 0
	v_accvgpr_write_b32 a13, 0
	v_accvgpr_write_b32 a14, 0
	v_accvgpr_write_b32 a15, 0
	v_accvgpr_write_b32 a16, 0
	v_accvgpr_write_b32 a17, 0
	v_accvgpr_write_b32 a18, 0
	v_accvgpr_write_b32 a19, 0
	v_accvgpr_write_b32 a20, 0
	v_accvgpr_write_b32 a21, 0
	v_accvgpr_write_b32 a22, 0
	v_accvgpr_write_b32 a23, 0
	v_accvgpr_write_b32 a24, 0
	v_accvgpr_write_b32 a25, 0
	v_accvgpr_write_b32 a26, 0
	v_accvgpr_write_b32 a27, 0
	v_accvgpr_write_b32 a28, 0
	v_accvgpr_write_b32 a29, 0
	v_accvgpr_write_b32 a30, 0
	v_accvgpr_write_b32 a31, 0
	v_accvgpr_write_b32 a32, 0
	v_accvgpr_write_b32 a33, 0
	v_accvgpr_write_b32 a34, 0
	v_accvgpr_write_b32 a35, 0
	v_accvgpr_write_b32 a36, 0
	v_accvgpr_write_b32 a37, 0
	v_accvgpr_write_b32 a38, 0
	v_accvgpr_write_b32 a39, 0
	v_mov_b32_e32 v2, 0
	v_mov_b32_e32 v3, 0
	v_mov_b32_e32 v4, 0
	v_mov_b32_e32 v5, 0
	v_lshrrev_b32_e32 v44, 1, v46
	v_subrev_u32_e32 v44, s17, v44
	v_and_b32_e32 v44, 63, v44
	v_lshlrev_b32_e32 v44, 5, v44
	v_and_b32_e32 v45, 1, v46
	v_lshl_or_b32 v44, v45, 4, v44
	v_xor_b32_e32 v45, 0x400, v44
	s_mul_i32 s23, s15, 0x1900
	s_add_u32 s23, s23, 0x11000
	v_add_u32_e32 v44, s23, v44
	v_add_u32_e32 v45, s23, v45
	v_add_u32_e32 v47, s23, v1
	ds_write_b128 v47, v[2:5] offset:4096
	ds_write_b128 v47, v[2:5] offset:5120
	s_waitcnt vmcnt(4)
	ds_write_b128 v44, v[48:51]
	ds_write_b128 v45, v[52:55]
	ds_write_b128 v44, v[56:59] offset:2048
	ds_write_b128 v45, v[60:63] offset:2048
	v_cvt_f16_f32_e32 v42, v42
	v_cvt_f16_f32_e32 v43, v43
	s_mov_b32 s28, 0x5040100
	v_perm_b32 v42, v42, v42, s28
	v_perm_b32 v43, v43, v43, s28
	v_lshrrev_b32_e32 v44, 5, v46
	v_and_b32_e32 v45, 15, v46
	v_bfe_u32 v47, v46, 4, 1
	v_cmp_eq_u32_e32 vcc, v45, v47
	v_lshlrev_b32_e32 v44, 4, v44
	v_add_u32_e32 v46, s23, v44
	v_add_u32_e32 v45, 0x800, v46
	v_mov_b32_e32 v47, s23
	v_add_u32_e32 v47, 0x1000, v47
	v_cndmask_b32_e32 v47, v47, v45, vcc
	s_waitcnt lgkmcnt(0)
	ds_read_b128 v[144:147], v46
	ds_read_b128 v[148:151], v46 offset:32
	ds_read_b128 v[160:163], v47
	ds_read_b128 v[152:155], v46 offset:64
	ds_read_b128 v[164:167], v47 offset:32
	s_add_u32 s27, s17, 4
	s_lshl_b32 s27, s27, 10
	s_add_u32 s29, s17, 63
	s_lshl_b32 s29, s29, 10
	s_movk_i32 s28, 0x400
	s_mov_b32 s26, 0
	s_waitcnt lgkmcnt(4)
	v_pk_max_u16 v128, v144, v42
	v_pk_max_u16 v129, v145, v42
	v_pk_max_u16 v130, v146, v42
	v_pk_max_u16 v131, v147, v42
	v_pk_max_u16 v136, v144, v43
	v_pk_max_u16 v137, v145, v43
	v_pk_max_u16 v138, v146, v43
	v_pk_max_u16 v139, v147, v43
	s_mov_b32 s31, 0xfc00
.Lk2_loop:
	s_and_b32 s23, s27, s31
	s_add_u32 s24, s20, s23
	s_addc_u32 s25, s21, 0
	s_add_u32 s27, s27, s28
	s_waitcnt vmcnt(3)
	s_waitcnt lgkmcnt(2)
	v_mfma_f32_32x32x16_f16 a[0:15], v[64:67], v[128:131], a[0:15]
	v_pk_max_u16 v132, v148, v42
	v_pk_max_u16 v133, v149, v42
	v_pk_max_u16 v134, v150, v42
	v_pk_max_u16 v135, v151, v42
	v_mfma_f32_32x32x16_f16 a[16:31], v[64:67], v[136:139], a[16:31]
	v_pk_max_u16 v140, v148, v43
	v_pk_max_u16 v141, v149, v43
	v_pk_max_u16 v142, v150, v43
	v_pk_max_u16 v143, v151, v43
	v_mfma_f32_16x16x32_f16 a[32:35], v[160:163], v[128:131], a[32:35]
	global_load_dwordx4 v[64:67], v1, s[24:25]
	ds_read_b128 v[156:159], v46 offset:96
	ds_read_b128 v[168:171], v47 offset:64
	v_mfma_f32_16x16x32_f16 a[36:39], v[160:163], v[136:139], a[36:39]
	s_and_b32 s23, s27, s31
	s_add_u32 s24, s20, s23
	s_addc_u32 s25, s21, 0
	s_add_u32 s27, s27, s28
	s_waitcnt vmcnt(3)
	s_waitcnt lgkmcnt(2)
	v_mfma_f32_32x32x16_f16 a[0:15], v[68:71], v[132:135], a[0:15]
	v_pk_max_u16 v128, v152, v42
	v_pk_max_u16 v129, v153, v42
	v_pk_max_u16 v130, v154, v42
	v_pk_max_u16 v131, v155, v42
	v_mfma_f32_32x32x16_f16 a[16:31], v[68:71], v[140:143], a[16:31]
	v_pk_max_u16 v136, v152, v43
	v_pk_max_u16 v137, v153, v43
	v_pk_max_u16 v138, v154, v43
	v_pk_max_u16 v139, v155, v43
	v_mfma_f32_16x16x32_f16 a[32:35], v[164:167], v[132:135], a[32:35]
	global_load_dwordx4 v[68:71], v1, s[24:25]
	ds_read_b128 v[144:147], v46 offset:128
	ds_read_b128 v[172:175], v47 offset:96
	v_mfma_f32_16x16x32_f16 a[36:39], v[164:167], v[140:143], a[36:39]
	s_and_b32 s23, s27, s31
	s_add_u32 s24, s20, s23
	s_addc_u32 s25, s21, 0
	s_add_u32 s27, s27, s28
	s_waitcnt vmcnt(3)
	s_waitcnt lgkmcnt(2)
	v_mfma_f32_32x32x16_f16 a[0:15], v[72:75], v[128:131], a[0:15]
	v_pk_max_u16 v132, v156, v42
	v_pk_max_u16 v133, v157, v42
	v_pk_max_u16 v134, v158, v42
	v_pk_max_u16 v135, v159, v42
	v_mfma_f32_32x32x16_f16 a[16:31], v[72:75], v[136:139], a[16:31]
	v_pk_max_u16 v140, v156, v43
	v_pk_max_u16 v141, v157, v43
	v_pk_max_u16 v142, v158, v43
	v_pk_max_u16 v143, v159, v43
	v_mfma_f32_16x16x32_f16 a[32:35], v[168:171], v[128:131], a[32:35]
	global_load_dwordx4 v[72:75], v1, s[24:25]
	ds_read_b128 v[148:151], v46 offset:160
	ds_read_b128 v[160:163], v47 offset:128
	v_mfma_f32_16x16x32_f16 a[36:39], v[168:171], v[136:139], a[36:39]
	s_and_b32 s23, s27, s31
	s_add_u32 s24, s20, s23
	s_addc_u32 s25, s21, 0
	s_add_u32 s27, s27, s28
	s_waitcnt vmcnt(3)
	s_waitcnt lgkmcnt(2)
	v_mfma_f32_32x32x16_f16 a[0:15], v[76:79], v[132:135], a[0:15]
	v_pk_max_u16 v128, v144, v42
	v_pk_max_u16 v129, v145, v42
	v_pk_max_u16 v130, v146, v42
	v_pk_max_u16 v131, v147, v42
	v_mfma_f32_32x32x16_f16 a[16:31], v[76:79], v[140:143], a[16:31]
	v_pk_max_u16 v136, v144, v43
	v_pk_max_u16 v137, v145, v43
	v_pk_max_u16 v138, v146, v43
	v_pk_max_u16 v139, v147, v43
	v_mfma_f32_16x16x32_f16 a[32:35], v[172:175], v[132:135], a[32:35]
	global_load_dwordx4 v[76:79], v1, s[24:25]
	ds_read_b128 v[152:155], v46 offset:192
	ds_read_b128 v[164:167], v47 offset:160
	v_mfma_f32_16x16x32_f16 a[36:39], v[172:175], v[140:143], a[36:39]
	s_add_u32 s26, s26, 1
	v_add_u32_e32 v46, 128, v46
	v_add_u32_e32 v47, 128, v47
	s_cmp_eq_u32 s26, 15
	s_cselect_b32 s27, s29, s27
	s_cselect_b32 s28, 0, s28
	s_cmp_lt_u32 s26, 16
	s_cbranch_scc1 .Lk2_loop
	v_and_b32_e32 v2, 63, v0
	v_lshrrev_b32_e32 v3, 5, v2
	v_and_b32_e32 v4, 31, v0
	s_lshl_b32 s23, s15, 4
	v_add_u32_e32 v3, s23, v3
	v_mul_u32_u24_e32 v3, 0x210, v3
	v_lshl_add_u32 v3, v4, 4, v3
	v_cmp_gt_u32_e32 vcc, 16, v2
	ds_write_b128 v3, a[0:3]
	ds_write_b128 v3, a[16:19] offset:4224
	ds_write_b128 v3, a[4:7] offset:1056
	ds_write_b128 v3, a[20:23] offset:5280
	ds_write_b128 v3, a[8:11] offset:2112
	ds_write_b128 v3, a[24:27] offset:6336
	ds_write_b128 v3, a[12:15] offset:3168
	ds_write_b128 v3, a[28:31] offset:7392
	s_and_saveexec_b64 s[2:3], vcc
	s_cbranch_execz .Lk2_nodred
	v_lshlrev_b32_e32 v5, 2, v2
	s_lshl_b32 s23, s15, 8
	v_add_u32_e32 v5, s23, v5
	v_add_u32_e32 v5, 0x10800, v5
	ds_write2_b32 v5, a32, a33 offset1:16
	ds_write2_b32 v5, a36, a37 offset0:32 offset1:48
